# adds: P8 partial last round spreads its units over all XCDs (block round-robin), full rounds keep the XCD-grouped permutation
# speedup vs baseline: 1.0052x; 1.0030x over previous
; #define LAS __attribute__((address_space(3)))
; #define PG8_STAGE(bufoff, gbase, voff) do { _Pragma("unroll") for (int _i = 0; _i < 2; ++_i) \
;         __builtin_amdgcn_global_load_lds((const unsigned*)((const char*)(gbase) + (voff)[_i]), (LAS unsigned*)(lds + (bufoff) + ldsw + _i * 8192), 16, 0, 0); } while (0)
; #define PG8_WAIT_V(n) asm volatile("s_waitcnt vmcnt(" #n ")" ::: "memory")
; template <class Epi, class Sched, bool GATHER, bool FP8>
; __device__ __forceinline__ void gemm_phase(LAS uchar* lds, const int K, const int LDA, const int LDB, const size_t kstepA, const size_t kstepB, const Sched& S, const Epi& E) {
;     ...
;     Unit cur, nxt; int ui = 0;
;     if (!S.next(0, cur)) return;
;     f32x4 acc[2][2][4][2];
; #pragma unroll
;     for (int a = 0; a < 2; ++a)
; #pragma unroll
;         for (int b = 0; b < 2; ++b)
; #pragma unroll
;             for (int m = 0; m < 4; ++m)
; #pragma unroll
;                 for (int n = 0; n < 2; ++n) acc[a][b][m][n] = (f32x4){0.f, 0.f, 0.f, 0.f};
;     bf16x8 At[4][2], B0[2][2], B1[2][2];
;     const char* cA = cur.pa; const char* cB = cur.pb;
;     if constexpr (GATHER) S.gather(cur, voA, (const LAS int*)nullptr);
;     PG8_STAGE(PG8_SB(0, 0), cB, voffB); PG8_STAGE(PG8_SB(0, 1), cB + hstep, voffB); PG8_STAGE(PG8_SA(0, 0), cA, voA[0]); PG8_STAGE(PG8_SA(0, 1), cA, voA[1]);
;     if (wr == 1) PG8_BAR;
;     PG8_WAIT_V(2); PG8_BAR;
;     PG8_STAGE(PG8_SB(1, 0), cB + kstepB, voffB); PG8_STAGE(PG8_SA(1, 0), cA + kstepA, voA[0]); PG8_STAGE(PG8_SB(1, 1), cB + hstep + kstepB, voffB);
;     __device__ __forceinline__ bool next(int i, pg8::Unit& u) const {
;         const int NB = __builtin_amdgcn_readfirstlane(tab[0]); const int L = i * G + c; if (L >= NB * nN) return false;
;         const int b = L / nN, pn = L - b * nN, e = __builtin_amdgcn_readfirstlane(tab[64 + b]);
;         u.pa = A; u.pb = B + (size_t)e * bexp + (size_t)pn * 256 * 128; u.row0 = b * 256; u.col0 = pn * 256; u.aux = e; u.blk = b; return true;
;     }
;     __device__ __forceinline__ void gather(const pg8::Unit& u, unsigned (&vo)[2][2], const LAS int*) const {
; #pragma unroll
;         for (int i = 0; i < 2; ++i) { int R, C; pg8::stage_rc((int)threadIdx.x * 16 + i * 8192, R, C);
; #pragma unroll
;             for (int h = 0; h < 2; ++h) vo[h][i] = (unsigned)(u.row0 + h * 128 + R) * (unsigned)W8LD + (unsigned)C * 2u; }
;     }
.LBB0_1022:
	s_add_i32 s4, 0, 0x22000
	v_mov_b32_e32 v2, s4
	ds_read_b32 v2, v2
	v_readfirstlane_b32 s18, v0
	s_waitcnt lgkmcnt(0)
	v_readfirstlane_b32 s4, v2
	s_lshl_b32 s4, s4, 3
	s_and_b32 s98, s87, 7
	s_lshl_b32 s98, s98, 5
	s_lshr_b32 s99, s87, 3
	s_or_b32 s98, s98, s99
	s_cmpk_eq_i32 s92, 0x100
	s_cselect_b32 s98, s98, s87
	s_lshr_b32 s101, s87, 6
	s_lshl_b32 s101, s101, 6
	s_and_b32 s99, s87, 7
	s_lshl_b32 s99, s99, 3
	s_or_b32 s101, s101, s99
	s_bfe_u32 s99, s87, 0x30003
	s_or_b32 s101, s101, s99
	s_cmpk_eq_i32 s92, 0x100
	s_cselect_b32 s101, s101, s87
	s_cmp_ge_i32 s98, s4
	s_cbranch_scc1 .LBB0_1041
	v_lshlrev_b32_e32 v3, 4, v0
	v_and_b32_e32 v2, 32, v0
	v_bitop3_b32 v2, v3, v2, 48 bitop3:0x6c
	v_or_b32_e32 v3, 0x2000, v3
	v_bfe_u32 v5, v0, 2, 4
	v_lshrrev_b32_e32 v6, 7, v3
	s_movk_i32 s8, 0x70
	s_add_u32 s4, s90, 0x1c000000
	v_and_or_b32 v216, v6, s8, v5
	v_lshrrev_b32_e32 v6, 5, v0
	s_addc_u32 s5, s91, 0
	v_and_or_b32 v195, v0, 64, v2
	v_and_b32_e32 v2, 48, v0
	v_and_b32_e32 v6, 4, v6
	v_bfe_u32 v7, v0, 2, 2
	s_add_u32 s23, s90, 0x50000000
	v_or3_b32 v6, v7, v6, v2
	v_lshrrev_b32_e32 v3, 6, v3
	s_movk_i32 s8, 0xc0
	s_addc_u32 s33, s91, 0
	v_and_or_b32 v3, v3, s8, v6
	s_ashr_i32 s8, s98, 31
	s_lshr_b32 s8, s8, 29
	s_add_i32 s8, s98, s8
	s_ashr_i32 s10, s8, 3
	s_lshl_b32 s9, s10, 2
	s_add_i32 s9, s9, 0
	s_add_i32 s9, s9, 0x22100
	v_lshl_or_b32 v196, v3, 7, v195
	v_mov_b32_e32 v3, s9
	ds_read_b32 v3, v3
	s_lshr_b32 s16, s18, 6
	s_and_b32 s8, s8, -8
	s_lshr_b32 s17, s18, 8
	s_lshl_b32 s44, s16, 10
	s_waitcnt lgkmcnt(0)
	v_readfirstlane_b32 s34, v3
	s_ashr_i32 s35, s34, 31
	s_sub_i32 s14, s98, s8
	s_lshl_b64 s[8:9], s[34:35], 22
	s_add_u32 s11, s23, s8
	s_addc_u32 s12, s33, s9
	s_ashr_i32 s15, s14, 31
	s_lshl_b64 s[8:9], s[14:15], 15
	v_lshrrev_b32_e32 v4, 2, v0
	s_add_u32 s36, s11, s8
	v_and_or_b32 v4, v4, 64, v6
	s_addc_u32 s37, s12, s9
	s_lshl_b32 s69, s10, 8
	v_lshl_or_b32 v198, v4, 7, v195
	s_movk_i32 s45, 0x80
	v_or_b32_e32 v4, s69, v216
	v_mul_lo_u32 v4, v4, s45
	v_or_b32_e32 v219, 0x80, v216
	s_add_i32 s46, s44, 0
	v_or_b32_e32 v202, v4, v195
	v_or_b32_e32 v4, s69, v219
	s_add_i32 s47, s46, 0x10000
	v_mov_b32_e32 v201, 0
	v_lshrrev_b32_e32 v3, 3, v0
	v_mul_lo_u32 v4, v4, s45
	v_mov_b32_e32 v199, v201
	s_mov_b32 m0, s47
	s_add_i32 s48, s46, 0x12000
	v_and_or_b32 v217, v3, 48, v5
	v_or_b32_e32 v204, v4, v195
	v_lshl_add_u64 v[4:5], s[36:37], 0, v[198:199]
	global_load_lds_dwordx4 v198, s[36:37]
	v_mov_b32_e32 v197, v201
	s_mov_b32 m0, s48
	s_add_i32 s49, s46, 0x14000
	s_mov_b64 s[8:9], 0x400
	v_or_b32_e32 v3, s69, v217
	v_lshl_add_u64 v[6:7], s[36:37], 0, v[196:197]
	global_load_lds_dwordx4 v196, s[36:37]
	v_lshl_add_u64 v[4:5], v[4:5], 0, s[8:9]
	s_mov_b32 m0, s49
	s_add_i32 s50, s46, 0x16000
	v_mul_lo_u32 v3, v3, s45
	v_or_b32_e32 v218, 0x80, v217
	global_load_lds_dwordx4 v[4:5], off
	v_lshl_add_u64 v[4:5], v[6:7], 0, s[8:9]
	s_mov_b32 m0, s50
	v_or_b32_e32 v200, v3, v195
	v_or_b32_e32 v3, s69, v218
	global_load_lds_dwordx4 v[4:5], off
	s_mov_b32 m0, s46
	s_add_i32 s51, s46, 0x2000
	v_mul_lo_u32 v3, v3, s45
	global_load_lds_dwordx4 v200, s[4:5]
	s_mov_b32 m0, s51
	s_add_i32 s52, s46, 0x4000
	v_or_b32_e32 v3, v3, v195
	global_load_lds_dwordx4 v202, s[4:5]
	s_mov_b32 m0, s52
	s_add_i32 s53, s46, 0x6000
	global_load_lds_dwordx4 v3, s[4:5]
	s_mov_b32 m0, s53
	s_load_dwordx2 s[10:11], s[0:1], 0x88
	global_load_lds_dwordx4 v204, s[4:5]
	s_cmp_eq_u32 s17, 1
	s_mov_b32 s54, 0x10000
	s_cselect_b64 s[12:13], -1, 0
	s_cmp_lg_u32 s17, 1
	v_mov_b32_e32 v203, v201
	s_cbranch_scc1 .LBB0_1025
	s_barrier

; template <class Epi, class Sched, bool GATHER, bool FP8>
; __device__ __forceinline__ void gemm_phase(LAS uchar* lds, const int K, const int LDA, const int LDB, const size_t kstepA, const size_t kstepB, const Sched& S, const Epi& E) {
;     ...
;         const bool has_next = S.next(ui + 1, nxt);
;         if constexpr (GATHER) { if (has_next) S.prefetch(nxt, lds + LDS_IDX + ((ui + 1) & 1) * 1024, wid, lane); }
;         E.prefetch(cur, lds + LDS_BIAS + (ui & 1) * 1024, wid, lane);
;         const char* nA = has_next ? nxt.pa : cA; const char* nB = has_next ? nxt.pb : cB;
;     __device__ __forceinline__ bool next(int i, pg8::Unit& u) const {
;         const int NB = __builtin_amdgcn_readfirstlane(tab[0]); const int L = i * G + c; if (L >= NB * nN) return false;
;         const int b = L / nN, pn = L - b * nN, e = __builtin_amdgcn_readfirstlane(tab[64 + b]);
;         u.pa = A; u.pb = B + (size_t)e * bexp + (size_t)pn * 256 * 128; u.row0 = b * 256; u.col0 = pn * 256; u.aux = e; u.blk = b; return true;
.LBB0_1028:
	ds_read_b32 v2, v221
	s_add_i32 s67, s38, 1
	s_mul_i32 s31, s67, s92
	s_nop 0
	s_waitcnt lgkmcnt(0)
	v_readfirstlane_b32 s28, v2
	s_lshl_b32 s35, s28, 3
	s_add_i32 s99, s31, 0x100
	s_cmp_gt_i32 s99, s35
	s_cselect_b32 s99, s101, s98
	s_add_i32 s31, s31, s99
	s_cmp_lt_i32 s31, s35
	s_cselect_b64 s[28:29], -1, 0
	s_cmp_ge_i32 s31, s35
	s_cbranch_scc1 .LBB0_1030
	s_ashr_i32 s24, s31, 31
	s_lshr_b32 s24, s24, 29
	s_add_i32 s24, s31, s24
	s_ashr_i32 s35, s24, 3
	s_lshl_b32 s25, s35, 2
	s_add_i32 s25, s25, 0
	s_add_i32 s25, s25, 0x22100
	v_mov_b32_e32 v2, s25
	ds_read_b32 v2, v2
	s_and_b32 s24, s24, -8
	s_sub_i32 s40, s31, s24
	s_waitcnt lgkmcnt(0)
	v_readfirstlane_b32 s24, v2
	s_ashr_i32 s25, s24, 31
	s_lshl_b64 s[26:27], s[24:25], 22
	s_add_u32 s25, s23, s26
	s_addc_u32 s31, s33, s27
	s_ashr_i32 s41, s40, 31
	s_lshl_b64 s[26:27], s[40:41], 15
	s_add_u32 s26, s25, s26
	s_addc_u32 s27, s31, s27
	s_lshl_b32 s68, s35, 8
	s_lshl_b32 s25, s40, 8
